# rwkv_chunk_pre boundary-row loads: load straight into the target register, drop the in-branch vmcnt(0) stalls, apply the bf16->f32 shift after the existing counted waits (6 sites)
# speedup vs baseline: 1.0179x; 1.0055x over previous
.LBB0_646:
	s_and_b32 s11, s4, 3
	s_lshl_b32 s33, s11, 6
	s_add_i32 s2, s3, -15
	s_and_b64 s[0:1], s[24:25], exec
	s_cselect_b32 s9, s3, s2
	v_readlane_b32 s2, v251, 11
	v_readlane_b32 s3, v251, 12
	s_load_dwordx4 s[68:71], s[2:3], 0x110
	s_add_i32 s10, s9, s8
	s_add_i32 s0, s10, -1
	s_mul_hi_i32 s1, s0, 0x1c00
	s_mulk_i32 s0, 0x1c00
	s_waitcnt lgkmcnt(0)
	s_add_u32 s0, s70, s0
	s_addc_u32 s1, s71, s1
	s_cmp_gt_i32 s9, 0
	s_cselect_b64 s[2:3], -1, 0
	s_add_i32 s9, s9, 16
	v_cndmask_b32_e64 v2, 0, 1, s[24:25]
	s_cmp_lt_i32 s9, s20
	v_cmp_ne_u32_e64 s[68:69], 1, v2
	v_cndmask_b32_e64 v2, 0, 1, s[2:3]
	s_cselect_b64 s[8:9], -1, 0
	s_andn2_b64 vcc, exec, s[24:25]
	v_cmp_ne_u32_e64 s[70:71], 1, v2
	s_cbranch_vccnz .LBB0_652
	global_load_dword v4, v[52:53], off offset:3584
	v_mov_b32_e32 v5, 0
	s_and_b64 vcc, exec, s[70:71]
	v_lshlrev_b32_e32 v162, 1, v48
	v_mov_b32_e32 v6, 0
	s_cbranch_vccnz .LBB0_649
	v_lshl_add_u64 v[2:3], s[0:1], 0, v[162:163]
	v_add_co_u32_e32 v2, vcc, 0x27401000, v2
	s_nop 1
	v_addc_co_u32_e32 v3, vcc, 0, v3, vcc
	global_load_ushort v6, v[2:3], off offset:768
.LBB0_649:
	v_lshl_add_u64 v[2:3], s[0:1], 0, v[162:163]
	v_add_co_u32_e32 v8, vcc, 0x27402000, v2
	s_nop 1
	v_addc_co_u32_e32 v9, vcc, 0, v3, vcc
	global_load_ushort v7, v[8:9], off offset:3840
	v_add_co_u32_e32 v8, vcc, 0x27404000, v2
	s_nop 1
	v_addc_co_u32_e32 v9, vcc, 0, v3, vcc
	v_add_co_u32_e32 v10, vcc, 0x27406000, v2
	global_load_ushort v8, v[8:9], off offset:2816
	s_nop 0
	v_addc_co_u32_e32 v11, vcc, 0, v3, vcc
	global_load_ushort v9, v[10:11], off offset:1792
	v_add_co_u32_e32 v10, vcc, 0x27408000, v2
	s_nop 1
	v_addc_co_u32_e32 v11, vcc, 0, v3, vcc
	v_add_co_u32_e32 v12, vcc, 0x27409000, v2
	global_load_ushort v10, v[10:11], off offset:768
	s_nop 0
	v_addc_co_u32_e32 v13, vcc, 0, v3, vcc
	global_load_ushort v11, v[12:13], off offset:3840
	v_add_co_u32_e32 v12, vcc, 0x2740b000, v2
	s_nop 1
	v_addc_co_u32_e32 v13, vcc, 0, v3, vcc
	v_add_co_u32_e32 v14, vcc, 0x2740d000, v2
	global_load_ushort v12, v[12:13], off offset:2816
	s_nop 0
	v_addc_co_u32_e32 v15, vcc, 0, v3, vcc
	global_load_ushort v13, v[14:15], off offset:1792
	v_add_co_u32_e32 v14, vcc, 0x2740f000, v2
	s_nop 1
	v_addc_co_u32_e32 v15, vcc, 0, v3, vcc
	v_add_co_u32_e32 v16, vcc, 0x27410000, v2
	global_load_ushort v14, v[14:15], off offset:768
	s_nop 0
	v_addc_co_u32_e32 v17, vcc, 0, v3, vcc
	global_load_ushort v15, v[16:17], off offset:3840
	v_add_co_u32_e32 v16, vcc, 0x27412000, v2
	s_nop 1
	v_addc_co_u32_e32 v17, vcc, 0, v3, vcc
	v_add_co_u32_e32 v18, vcc, 0x27414000, v2
	global_load_ushort v16, v[16:17], off offset:2816
	s_nop 0
	v_addc_co_u32_e32 v19, vcc, 0, v3, vcc
	global_load_ushort v17, v[18:19], off offset:1792
	v_add_co_u32_e32 v18, vcc, 0x27416000, v2
	s_nop 1
	v_addc_co_u32_e32 v19, vcc, 0, v3, vcc
	v_add_co_u32_e32 v20, vcc, 0x27417000, v2
	global_load_ushort v18, v[18:19], off offset:768
	s_nop 0
	v_addc_co_u32_e32 v21, vcc, 0, v3, vcc
	global_load_ushort v19, v[20:21], off offset:3840
	v_add_co_u32_e32 v20, vcc, 0x27419000, v2
	s_nop 1
	v_addc_co_u32_e32 v21, vcc, 0, v3, vcc
	v_add_co_u32_e32 v22, vcc, 0x2741b000, v2
	global_load_ushort v20, v[20:21], off offset:2816
	s_nop 0
	v_addc_co_u32_e32 v23, vcc, 0, v3, vcc
	global_load_ushort v21, v[22:23], off offset:1792
	v_add_co_u32_e32 v22, vcc, 0x2741d000, v2
	s_nop 1
	v_addc_co_u32_e32 v23, vcc, 0, v3, vcc
	global_load_ushort v22, v[22:23], off offset:768
	s_andn2_b64 vcc, exec, s[8:9]
	s_cbranch_vccnz .LBB0_651
	v_add_co_u32_e32 v2, vcc, 0x2741e000, v2
	s_nop 1
	v_addc_co_u32_e32 v3, vcc, 0, v3, vcc
	global_load_ushort v5, v[2:3], off offset:3840
.LBB0_651:
	s_waitcnt vmcnt(14)
	v_lshlrev_b32_e32 v6, 16, v6
	v_lshlrev_b32_e32 v3, 16, v8
	v_lshlrev_b32_e32 v2, 16, v7
	v_add_f32_e32 v6, v6, v3
	v_fma_f32 v6, v6, 0.5, -v2
	v_fma_f32 v6, v4, v6, v2
	v_mul_f32_e32 v6, 0xbfb8aa3b, v6
	v_exp_f32_e32 v6, v6
	s_waitcnt vmcnt(13)
	v_lshlrev_b32_e32 v7, 16, v9
	v_add_f32_e32 v2, v2, v7
	s_waitcnt vmcnt(12)
	v_lshlrev_b32_e32 v8, 16, v10
	v_add_f32_e32 v6, 1.0, v6
	v_rcp_f32_e32 v6, v6
	v_fma_f32 v2, v2, 0.5, -v3
	s_waitcnt vmcnt(11)
	v_lshlrev_b32_e32 v9, 16, v11
	v_fma_f32 v2, v4, v2, v3
	v_add_u32_e32 v6, 0x8000, v6
	v_add_f32_e32 v3, v3, v8
	ds_write_b16_d16_hi v51, v6 offset:2304
	v_fma_f32 v3, v3, 0.5, -v7
	v_add_f32_e32 v6, v7, v9
	v_mul_f32_e32 v2, 0xbfb8aa3b, v2
	v_fma_f32 v3, v4, v3, v7
	v_fma_f32 v6, v6, 0.5, -v8
	v_exp_f32_e32 v2, v2
	v_mul_f32_e32 v3, 0xbfb8aa3b, v3
	v_fma_f32 v6, v4, v6, v8
	v_exp_f32_e32 v3, v3
	v_mul_f32_e32 v6, 0xbfb8aa3b, v6
	v_exp_f32_e32 v6, v6
	v_add_f32_e32 v2, 1.0, v2
	v_rcp_f32_e32 v2, v2
	v_add_f32_e32 v3, 1.0, v3
	v_rcp_f32_e32 v3, v3
	v_add_f32_e32 v6, 1.0, v6
	v_rcp_f32_e32 v6, v6
	v_add_u32_e32 v2, 0x8000, v2
	s_waitcnt vmcnt(10)
	v_lshlrev_b32_e32 v10, 16, v12
	s_waitcnt vmcnt(9)
	v_lshlrev_b32_e32 v11, 16, v13
	ds_write_b16_d16_hi v51, v2 offset:2448
	v_add_u32_e32 v2, 0x8000, v3
	ds_write_b16_d16_hi v51, v2 offset:2592
	v_add_u32_e32 v2, 0x8000, v6
	v_add_f32_e32 v3, v8, v10
	v_add_f32_e32 v6, v9, v11
	v_fma_f32 v3, v3, 0.5, -v9
	v_fma_f32 v6, v6, 0.5, -v10
	v_fma_f32 v3, v4, v3, v9
	v_fma_f32 v6, v4, v6, v10
	v_mul_f32_e32 v3, 0xbfb8aa3b, v3
	v_mul_f32_e32 v6, 0xbfb8aa3b, v6
	v_exp_f32_e32 v3, v3
	v_exp_f32_e32 v6, v6
	s_waitcnt vmcnt(8)
	v_lshlrev_b32_e32 v12, 16, v14
	ds_write_b16_d16_hi v51, v2 offset:2736
	v_add_f32_e32 v2, 1.0, v3
	v_add_f32_e32 v3, 1.0, v6
	v_add_f32_e32 v6, v10, v12
	v_fma_f32 v6, v6, 0.5, -v11
	v_fma_f32 v6, v4, v6, v11
	v_rcp_f32_e32 v2, v2
	v_mul_f32_e32 v6, 0xbfb8aa3b, v6
	v_rcp_f32_e32 v3, v3
	v_exp_f32_e32 v6, v6
	s_waitcnt vmcnt(7)
	v_lshlrev_b32_e32 v13, 16, v15
	v_add_u32_e32 v2, 0x8000, v2
	ds_write_b16_d16_hi v51, v2 offset:2880
	v_add_u32_e32 v2, 0x8000, v3
	v_add_f32_e32 v3, 1.0, v6
	v_add_f32_e32 v6, v11, v13
	v_fma_f32 v6, v6, 0.5, -v12
	v_fma_f32 v6, v4, v6, v12
	v_rcp_f32_e32 v3, v3
	v_mul_f32_e32 v6, 0xbfb8aa3b, v6
	v_exp_f32_e32 v6, v6
	s_waitcnt vmcnt(6)
	v_lshlrev_b32_e32 v14, 16, v16
	s_waitcnt vmcnt(5)
	v_lshlrev_b32_e32 v15, 16, v17
	ds_write_b16_d16_hi v51, v2 offset:3024
	v_add_u32_e32 v2, 0x8000, v3
	v_add_f32_e32 v3, v12, v14
	ds_write_b16_d16_hi v51, v2 offset:3168
	v_add_f32_e32 v2, 1.0, v6
	v_fma_f32 v3, v3, 0.5, -v13
	v_add_f32_e32 v6, v13, v15
	v_fma_f32 v3, v4, v3, v13
	v_fma_f32 v6, v6, 0.5, -v14
	v_mul_f32_e32 v3, 0xbfb8aa3b, v3
	v_fma_f32 v6, v4, v6, v14
	v_exp_f32_e32 v3, v3
	v_mul_f32_e32 v6, 0xbfb8aa3b, v6
	v_exp_f32_e32 v6, v6
	v_rcp_f32_e32 v2, v2
	v_add_f32_e32 v3, 1.0, v3
	v_rcp_f32_e32 v3, v3
	v_add_f32_e32 v6, 1.0, v6
	v_rcp_f32_e32 v6, v6
	v_add_u32_e32 v2, 0x8000, v2
	s_waitcnt vmcnt(4)
	v_lshlrev_b32_e32 v16, 16, v18
	s_waitcnt vmcnt(3)
	v_lshlrev_b32_e32 v17, 16, v19
	ds_write_b16_d16_hi v51, v2 offset:3312
	v_add_u32_e32 v2, 0x8000, v3
	ds_write_b16_d16_hi v51, v2 offset:3456
	v_add_u32_e32 v2, 0x8000, v6
	v_add_f32_e32 v3, v14, v16
	v_add_f32_e32 v6, v15, v17
	v_fma_f32 v3, v3, 0.5, -v15
	v_fma_f32 v6, v6, 0.5, -v16
	v_fma_f32 v3, v4, v3, v15
	v_fma_f32 v6, v4, v6, v16
	v_mul_f32_e32 v3, 0xbfb8aa3b, v3
	v_mul_f32_e32 v6, 0xbfb8aa3b, v6
	v_exp_f32_e32 v3, v3
	v_exp_f32_e32 v6, v6
	s_waitcnt vmcnt(2)
	v_lshlrev_b32_e32 v18, 16, v20
	ds_write_b16_d16_hi v51, v2 offset:3600
	v_add_f32_e32 v2, 1.0, v3
	v_add_f32_e32 v3, 1.0, v6
	v_add_f32_e32 v6, v16, v18
	v_fma_f32 v6, v6, 0.5, -v17
	v_fma_f32 v6, v4, v6, v17
	v_rcp_f32_e32 v2, v2
	v_mul_f32_e32 v6, 0xbfb8aa3b, v6
	v_rcp_f32_e32 v3, v3
	v_exp_f32_e32 v6, v6
	v_add_u32_e32 v2, 0x8000, v2
	ds_write_b16_d16_hi v51, v2 offset:3744
	v_add_u32_e32 v2, 0x8000, v3
	v_add_f32_e32 v3, 1.0, v6
	v_rcp_f32_e32 v3, v3
	s_waitcnt vmcnt(1)
	v_lshlrev_b32_e32 v19, 16, v21
	s_waitcnt vmcnt(0)
	v_lshlrev_b32_e32 v20, 16, v22
	v_lshlrev_b32_e32 v5, 16, v5
	v_add_f32_e32 v6, v17, v19
	v_fma_f32 v6, v6, 0.5, -v18
	ds_write_b16_d16_hi v51, v2 offset:3888
	v_add_u32_e32 v2, 0x8000, v3
	v_add_f32_e32 v3, v18, v20
	v_fma_f32 v6, v4, v6, v18
	v_fma_f32 v3, v3, 0.5, -v19
	v_add_f32_e32 v5, v5, v19
	v_mul_f32_e32 v6, 0xbfb8aa3b, v6
	v_fma_f32 v3, v4, v3, v19
	v_fma_f32 v5, v5, 0.5, -v20
	v_exp_f32_e32 v6, v6
	v_mul_f32_e32 v3, 0xbfb8aa3b, v3
	v_fmac_f32_e32 v20, v4, v5
	v_exp_f32_e32 v3, v3
	v_mul_f32_e32 v4, 0xbfb8aa3b, v20
	v_exp_f32_e32 v4, v4
	ds_write_b16_d16_hi v51, v2 offset:4032
	v_add_f32_e32 v2, 1.0, v6
	v_rcp_f32_e32 v2, v2
	v_add_f32_e32 v3, 1.0, v3
	v_rcp_f32_e32 v3, v3
	v_add_f32_e32 v4, 1.0, v4
	v_rcp_f32_e32 v4, v4
	v_add_u32_e32 v2, 0x8000, v2
	ds_write_b16_d16_hi v51, v2 offset:4176
	v_add_u32_e32 v2, 0x8000, v3
	ds_write_b16_d16_hi v51, v2 offset:4320
	v_add_u32_e32 v2, 0x8000, v4
	ds_write_b16_d16_hi v51, v2 offset:4464
	v_or_b32_e32 v10, s33, v78
	s_waitcnt lgkmcnt(0)
	v_lshlrev_b32_e32 v162, 7, v10
	ds_read_b128 v[2:5], v55 offset:2304
	ds_read_b128 v[6:9], v55 offset:2368
	s_waitcnt lgkmcnt(0)
	v_lshl_add_u64 v[18:19], v[60:61], 0, v[162:163]
	global_load_dwordx4 v[10:13], v[18:19], off
	global_load_dwordx4 v[14:17], v[18:19], off offset:64
	v_add_u32_e32 v20, s10, v54
	s_lshl_b32 s20, s33, 2
	v_ashrrev_i32_e32 v21, 31, v20
	v_lshl_add_u64 v[22:23], v[56:57], 0, s[20:21]
	s_movk_i32 s2, 0x1000
	s_waitcnt vmcnt(1) lgkmcnt(1)
	v_mfma_f32_16x16x32_bf16 v[10:13], v[2:5], v[10:13], 0
	s_waitcnt vmcnt(0) lgkmcnt(0)
	v_mfma_f32_16x16x32_bf16 v[10:13], v[6:9], v[14:17], v[10:13]
	v_lshlrev_b64 v[14:15], 10, v[20:21]
	v_lshl_add_u64 v[20:21], v[22:23], 0, v[14:15]
	s_nop 5
	global_store_dword v[20:21], v10, off
	global_store_dword v[20:21], v11, off offset:1024
	global_store_dword v[20:21], v12, off offset:2048
	global_store_dword v[20:21], v13, off offset:3072
	global_load_dwordx4 v[10:13], v[18:19], off offset:2048
	s_nop 0
	global_load_dwordx4 v[14:17], v[18:19], off offset:2112
	v_add_co_u32_e32 v18, vcc, s2, v18
	s_waitcnt vmcnt(1)
	v_mfma_f32_16x16x32_bf16 v[10:13], v[2:5], v[10:13], 0
	v_addc_co_u32_e32 v19, vcc, 0, v19, vcc
	s_waitcnt vmcnt(0)
	v_mfma_f32_16x16x32_bf16 v[10:13], v[6:9], v[14:17], v[10:13]
	s_nop 7
	global_store_dword v[20:21], v10, off offset:64
	global_store_dword v[20:21], v11, off offset:1088
	global_store_dword v[20:21], v12, off offset:2112
	global_store_dword v[20:21], v13, off offset:3136
	global_load_dwordx4 v[10:13], v[18:19], off
	s_nop 0
	global_load_dwordx4 v[14:17], v[18:19], off offset:64
	s_waitcnt vmcnt(1)
	v_mfma_f32_16x16x32_bf16 v[10:13], v[2:5], v[10:13], 0
	s_waitcnt vmcnt(0)
	v_mfma_f32_16x16x32_bf16 v[10:13], v[6:9], v[14:17], v[10:13]
	s_nop 7
	global_store_dword v[20:21], v10, off offset:128
	global_store_dword v[20:21], v11, off offset:1152
	global_store_dword v[20:21], v12, off offset:2176
	global_store_dword v[20:21], v13, off offset:3200
	global_load_dwordx4 v[10:13], v[18:19], off offset:2048
	s_nop 0
	global_load_dwordx4 v[14:17], v[18:19], off offset:2112
	s_waitcnt vmcnt(1)
	v_mfma_f32_16x16x32_bf16 v[2:5], v[2:5], v[10:13], 0
	s_waitcnt vmcnt(0)
	v_mfma_f32_16x16x32_bf16 v[2:5], v[6:9], v[14:17], v[2:5]
	s_nop 7
	global_store_dword v[20:21], v2, off offset:192
	global_store_dword v[20:21], v3, off offset:1216
	global_store_dword v[20:21], v4, off offset:2240
	global_store_dword v[20:21], v5, off offset:3264
.LBB0_652:
	s_add_u32 s2, s0, 0x27400c00
	s_addc_u32 s3, s1, 0
	s_ashr_i32 s20, s4, 5
	s_lshl_b32 s78, s20, 8
	v_or_b32_e32 v4, s33, v48
	s_add_i32 s78, s78, s94
	v_or_b32_e32 v2, s78, v4
	v_ashrrev_i32_e32 v3, 31, v2
	v_lshlrev_b64 v[2:3], 2, v[2:3]
	v_readlane_b32 vcc_lo, v254, 49
	v_lshl_add_u64 v[6:7], s[92:93], 0, v[2:3]
	v_lshl_add_u64 v[2:3], s[6:7], 0, v[2:3]
	v_or_b32_e32 v162, vcc_lo, v4
	global_load_dword v6, v[6:7], off
	s_andn2_b32 s4, s4, 31
	global_load_dword v7, v[2:3], off
	v_lshlrev_b64 v[2:3], 2, v[162:163]
	v_lshl_add_u64 v[8:9], s[38:39], 0, v[2:3]
	v_lshl_add_u64 v[10:11], s[84:85], 0, v[2:3]
	v_lshl_add_u64 v[2:3], s[12:13], 0, v[2:3]
	global_load_dword v8, v[8:9], off
	v_lshlrev_b32_e32 v162, 2, v4
	global_load_dword v9, v[10:11], off
	v_or_b32_e32 v5, 0x100, v4
	global_load_dword v10, v[2:3], off
	v_add_u32_e32 v2, s4, v87
	v_ashrrev_i32_e32 v3, 31, v2
	v_lshl_add_u64 v[16:17], v[2:3], 2, s[18:19]
	global_load_dword v14, v162, s[18:19]
	global_load_dword v13, v162, s[18:19] offset:1024
	global_load_dword v11, v162, s[18:19] offset:2048
	global_load_dword v12, v[16:17], off
	v_mov_b32_e32 v15, 0
	s_and_b64 vcc, exec, s[70:71]
	v_lshlrev_b32_e32 v16, 1, v4
	v_lshlrev_b32_e32 v21, 1, v5
	v_mov_b32_e32 v19, 0
	v_mov_b32_e32 v18, 0
	s_cbranch_vccnz .LBB0_654
	global_load_ushort v19, v16, s[2:3]
	global_load_ushort v18, v21, s[2:3]
.LBB0_654:
	v_or_b32_e32 v4, 0x200, v4
	s_and_b64 vcc, exec, s[70:71]
	v_lshlrev_b32_e32 v22, 1, v4
	v_mov_b32_e32 v20, 0
	s_cbranch_vccnz .LBB0_656
	v_lshl_add_u64 v[4:5], v[2:3], 1, s[2:3]
	global_load_ushort v20, v[4:5], off
	s_nop 0
	global_load_ushort v15, v22, s[2:3]
.LBB0_656:
	s_add_u32 s2, s0, 0x27402800
	s_addc_u32 s3, s1, 0
	v_lshlrev_b64 v[4:5], 1, v[2:3]
	global_load_ushort v23, v16, s[2:3]
	global_load_ushort v24, v21, s[2:3]
	global_load_ushort v25, v22, s[2:3]
	v_lshl_add_u64 v[26:27], s[2:3], 0, v[4:5]
	s_add_u32 s2, s0, 0x27404400
	s_addc_u32 s3, s1, 0
	global_load_ushort v26, v[26:27], off
	s_nop 0
	global_load_ushort v27, v16, s[2:3]
	global_load_ushort v28, v21, s[2:3]
	global_load_ushort v29, v22, s[2:3]
	v_lshl_add_u64 v[30:31], s[2:3], 0, v[4:5]
	s_add_u32 s2, s0, 0x27406000
	s_addc_u32 s3, s1, 0
	global_load_ushort v30, v[30:31], off
	s_nop 0
	global_load_ushort v31, v16, s[2:3]
	global_load_ushort v32, v21, s[2:3]
	global_load_ushort v33, v22, s[2:3]
	v_lshl_add_u64 v[34:35], s[2:3], 0, v[4:5]
	s_add_u32 s2, s0, 0x27407c00
	s_addc_u32 s3, s1, 0
	global_load_ushort v34, v[34:35], off
	s_nop 0
	global_load_ushort v35, v16, s[2:3]
	global_load_ushort v36, v21, s[2:3]
	global_load_ushort v37, v22, s[2:3]
	v_lshl_add_u64 v[38:39], s[2:3], 0, v[4:5]
	s_add_u32 s2, s0, 0x27409800
	s_addc_u32 s3, s1, 0
	global_load_ushort v38, v[38:39], off
	s_nop 0
	global_load_ushort v39, v16, s[2:3]
	global_load_ushort v40, v21, s[2:3]
	global_load_ushort v41, v22, s[2:3]
	v_lshl_add_u64 v[42:43], s[2:3], 0, v[4:5]
	s_add_u32 s2, s0, 0x2740b400
	s_addc_u32 s3, s1, 0
	global_load_ushort v42, v[42:43], off
	s_nop 0
	global_load_ushort v43, v16, s[2:3]
	global_load_ushort v44, v21, s[2:3]
	global_load_ushort v45, v22, s[2:3]
	v_lshl_add_u64 v[74:75], s[2:3], 0, v[4:5]
	s_add_u32 s2, s0, 0x2740d000
	s_addc_u32 s3, s1, 0
	global_load_ushort v58, v[74:75], off
	global_load_ushort v63, v16, s[2:3]
	global_load_ushort v65, v21, s[2:3]
	global_load_ushort v67, v22, s[2:3]
	v_lshl_add_u64 v[74:75], s[2:3], 0, v[4:5]
	s_add_u32 s2, s0, 0x2740ec00
	s_addc_u32 s3, s1, 0
	global_load_ushort v69, v[74:75], off
	global_load_ushort v71, v16, s[2:3]
	global_load_ushort v73, v21, s[2:3]
	s_nop 0
	global_load_ushort v74, v22, s[2:3]
	v_lshl_add_u64 v[76:77], s[2:3], 0, v[4:5]
	s_add_u32 s2, s0, 0x27410800
	s_addc_u32 s3, s1, 0
	global_load_ushort v75, v[76:77], off
	s_nop 0
	global_load_ushort v76, v16, s[2:3]
	global_load_ushort v77, v21, s[2:3]
	global_load_ushort v124, v22, s[2:3]
	v_lshl_add_u64 v[126:127], s[2:3], 0, v[4:5]
	s_add_u32 s2, s0, 0x27412400
	s_addc_u32 s3, s1, 0
	global_load_ushort v125, v[126:127], off
	s_nop 0
	global_load_ushort v126, v16, s[2:3]
	global_load_ushort v127, v21, s[2:3]
	global_load_ushort v128, v22, s[2:3]
	v_lshl_add_u64 v[130:131], s[2:3], 0, v[4:5]
	s_add_u32 s2, s0, 0x27414000
	s_addc_u32 s3, s1, 0
	global_load_ushort v129, v[130:131], off
	s_nop 0
	global_load_ushort v130, v16, s[2:3]
	global_load_ushort v131, v21, s[2:3]
	global_load_ushort v132, v22, s[2:3]
	v_lshl_add_u64 v[134:135], s[2:3], 0, v[4:5]
	s_add_u32 s2, s0, 0x27415c00
	s_addc_u32 s3, s1, 0
	global_load_ushort v133, v[134:135], off
	s_nop 0
	global_load_ushort v134, v16, s[2:3]
	global_load_ushort v135, v21, s[2:3]
	global_load_ushort v136, v22, s[2:3]
	v_lshl_add_u64 v[138:139], s[2:3], 0, v[4:5]
	s_add_u32 s2, s0, 0x27417800
	s_addc_u32 s3, s1, 0
	global_load_ushort v137, v[138:139], off
	s_nop 0
	global_load_ushort v138, v16, s[2:3]
	global_load_ushort v139, v21, s[2:3]
	global_load_ushort v140, v22, s[2:3]
	v_lshl_add_u64 v[142:143], s[2:3], 0, v[4:5]
	s_add_u32 s2, s0, 0x27419400
	s_addc_u32 s3, s1, 0
	global_load_ushort v141, v[142:143], off
	s_nop 0
	global_load_ushort v142, v16, s[2:3]
	global_load_ushort v143, v21, s[2:3]
	global_load_ushort v144, v22, s[2:3]
	v_lshl_add_u64 v[146:147], s[2:3], 0, v[4:5]
	s_add_u32 s2, s0, 0x2741b000
	s_addc_u32 s3, s1, 0
	global_load_ushort v145, v[146:147], off
	s_nop 0
	global_load_ushort v146, v16, s[2:3]
	global_load_ushort v147, v21, s[2:3]
	global_load_ushort v148, v22, s[2:3]
	v_lshl_add_u64 v[150:151], s[2:3], 0, v[4:5]
	s_add_u32 s2, s0, 0x2741cc00
	s_addc_u32 s3, s1, 0
	global_load_ushort v149, v[150:151], off
	s_nop 0
	global_load_ushort v150, v16, s[2:3]
	global_load_ushort v151, v21, s[2:3]
	global_load_ushort v152, v22, s[2:3]
	v_lshl_add_u64 v[4:5], s[2:3], 0, v[4:5]
	global_load_ushort v153, v[4:5], off
	s_add_u32 s0, s0, 0x2741e800
	v_cndmask_b32_e64 v5, 0, 1, s[8:9]
	s_addc_u32 s1, s1, 0
	v_mov_b32_e32 v4, 0
	v_cmp_ne_u32_e64 s[70:71], 1, v5
	s_andn2_b64 vcc, exec, s[8:9]
	v_mov_b32_e32 v17, 0
	v_mov_b32_e32 v5, 0
	s_cbranch_vccnz .LBB0_658
	global_load_ushort v17, v16, s[0:1]
	s_nop 0
	global_load_ushort v5, v21, s[0:1]
.LBB0_658:
	s_and_b64 vcc, exec, s[70:71]
	v_mov_b32_e32 v16, 0
	s_cbranch_vccnz .LBB0_660
	v_lshl_add_u64 v[2:3], v[2:3], 1, s[0:1]
	global_load_ushort v16, v[2:3], off
	s_nop 0
	global_load_ushort v4, v22, s[0:1]
.LBB0_660:
	s_waitcnt vmcnt(58)
	v_lshlrev_b32_e32 v19, 16, v19
	v_lshlrev_b32_e32 v18, 16, v18
	v_lshlrev_b32_e32 v20, 16, v20
	v_lshlrev_b32_e32 v15, 16, v15
	v_lshlrev_b32_e32 v159, 16, v28
	v_lshlrev_b32_e32 v155, 16, v24
	s_and_b64 s[0:1], s[24:25], exec
	v_add_f32_e32 v18, v18, v159
	s_cselect_b32 s0, 0, 15
	v_fma_f32 v18, v18, 0.5, -v155
	v_lshlrev_b32_e32 v158, 16, v27
	s_mul_i32 s1, s0, 0x90
	v_fma_f32 v18, v13, v18, v155
	v_lshlrev_b32_e32 v154, 16, v23
	s_waitcnt vmcnt(56)
	v_lshlrev_b32_e32 v161, 16, v30
	s_waitcnt vmcnt(55)
	v_lshlrev_b32_e32 v164, 16, v31
	s_waitcnt vmcnt(13)
	v_lshlrev_b32_e32 v31, 16, v140
	v_add_f32_e32 v19, v19, v158
	v_add_u32_e32 v140, s1, v51
	v_add_u32_e32 v18, 0x8000, v18
	v_lshlrev_b32_e32 v157, 16, v26
	v_fma_f32 v19, v19, 0.5, -v154
	ds_write_b16_d16_hi v140, v18
	v_add_f32_e32 v18, v20, v161
	v_fma_f32 v19, v14, v19, v154
	v_fma_f32 v18, v18, 0.5, -v157
	v_add_u32_e32 v19, 0x8000, v19
	v_fma_f32 v18, v12, v18, v157
	ds_write_b16_d16_hi v140, v19 offset:2304
	v_mul_f32_e32 v19, 0x4038aa3b, v18
	v_exp_f32_e32 v19, v19
	v_lshlrev_b32_e32 v160, 16, v29
	v_lshlrev_b32_e32 v156, 16, v25
	v_add_f32_e32 v15, v15, v160
	v_add_f32_e32 v19, 1.0, v19
	v_rcp_f32_e32 v19, v19
	v_fma_f32 v15, v15, 0.5, -v156
	v_fma_f32 v15, v11, v15, v156
	v_add_u32_e32 v15, 0x8000, v15
	v_lshl_add_u32 v20, s0, 7, v51
	ds_write_b16_d16_hi v20, v15 offset:13696
	v_fma_f32 v15, v19, -2.0, 1.0
	v_cndmask_b32_e64 v15, v18, v15, s[40:41]
	v_add_u32_e32 v15, 0x8000, v15
	ds_write_b16_d16_hi v140, v15 offset:4608
	v_add_f32_e32 v15, v154, v164
	s_cselect_b32 s0, 1, 14
	v_fma_f32 v15, v15, 0.5, -v158
	v_fma_f32 v15, v14, v15, v158
	s_mul_i32 s1, s0, 0x90
	v_lshlrev_b32_e32 v165, 16, v32
	v_add_u32_e32 v15, 0x8000, v15
	v_add_u32_e32 v18, s1, v51
	ds_write_b16_d16_hi v18, v15 offset:2304
	v_add_f32_e32 v15, v155, v165
	v_fma_f32 v15, v15, 0.5, -v159
	v_fma_f32 v15, v13, v15, v159
	v_lshlrev_b32_e32 v34, 16, v34
	v_add_u32_e32 v15, 0x8000, v15
	ds_write_b16_d16_hi v18, v15
	v_add_f32_e32 v15, v157, v34
	v_fma_f32 v15, v15, 0.5, -v161
	v_fma_f32 v15, v12, v15, v161
	v_mul_f32_e32 v19, 0x4038aa3b, v15
	v_exp_f32_e32 v19, v19
	v_lshlrev_b32_e32 v33, 16, v33
	v_lshlrev_b32_e32 v35, 16, v35
	v_add_f32_e32 v20, v156, v33
	v_add_f32_e32 v19, 1.0, v19
	v_rcp_f32_e32 v19, v19
	v_fma_f32 v20, v20, 0.5, -v160
	v_lshl_add_u32 v140, s0, 7, v51
	s_cselect_b32 s0, 2, 13
	v_fma_f32 v19, v19, -2.0, 1.0
	v_cndmask_b32_e64 v15, v15, v19, s[40:41]
	v_add_u32_e32 v15, 0x8000, v15
	ds_write_b16_d16_hi v18, v15 offset:4608
	v_add_f32_e32 v15, v158, v35
	v_fma_f32 v15, v15, 0.5, -v164
	v_fma_f32 v20, v11, v20, v160
	v_fma_f32 v15, v14, v15, v164
	s_mul_i32 s1, s0, 0x90
	v_lshlrev_b32_e32 v36, 16, v36
	v_add_u32_e32 v20, 0x8000, v20
	v_add_u32_e32 v15, 0x8000, v15
	v_add_u32_e32 v18, s1, v51
	ds_write_b16_d16_hi v140, v20 offset:13696
	ds_write_b16_d16_hi v18, v15 offset:2304
	v_add_f32_e32 v15, v159, v36
	v_fma_f32 v15, v15, 0.5, -v165
	v_fma_f32 v15, v13, v15, v165
	v_lshlrev_b32_e32 v38, 16, v38
	v_add_u32_e32 v15, 0x8000, v15
	ds_write_b16_d16_hi v18, v15
	v_add_f32_e32 v15, v161, v38
	v_fma_f32 v15, v15, 0.5, -v34
	v_fma_f32 v15, v12, v15, v34
	v_mul_f32_e32 v19, 0x4038aa3b, v15
	v_exp_f32_e32 v19, v19
	v_lshlrev_b32_e32 v37, 16, v37
	v_add_f32_e32 v20, v160, v37
	v_fma_f32 v20, v20, 0.5, -v33
	v_add_f32_e32 v19, 1.0, v19
	v_rcp_f32_e32 v19, v19
	v_fma_f32 v20, v11, v20, v33
	v_lshlrev_b32_e32 v39, 16, v39
	v_add_u32_e32 v20, 0x8000, v20
	v_fma_f32 v19, v19, -2.0, 1.0
	v_cndmask_b32_e64 v15, v15, v19, s[40:41]
	v_lshl_add_u32 v140, s0, 7, v51
	v_add_u32_e32 v15, 0x8000, v15
	ds_write_b16_d16_hi v140, v20 offset:13696
	ds_write_b16_d16_hi v18, v15 offset:4608
	v_add_f32_e32 v15, v164, v39
	s_cselect_b32 s0, 3, 12
	v_fma_f32 v15, v15, 0.5, -v35
	v_fma_f32 v15, v14, v15, v35
	s_mul_i32 s1, s0, 0x90
	v_lshlrev_b32_e32 v40, 16, v40
	v_add_u32_e32 v15, 0x8000, v15
	v_add_u32_e32 v18, s1, v51
	ds_write_b16_d16_hi v18, v15 offset:2304
	v_add_f32_e32 v15, v165, v40
	v_fma_f32 v15, v15, 0.5, -v36
	v_fma_f32 v15, v13, v15, v36
	v_lshlrev_b32_e32 v42, 16, v42
	v_add_u32_e32 v15, 0x8000, v15
	ds_write_b16_d16_hi v18, v15
	v_add_f32_e32 v15, v34, v42
	v_fma_f32 v15, v15, 0.5, -v38
	v_fma_f32 v15, v12, v15, v38
	v_mul_f32_e32 v19, 0x4038aa3b, v15
	v_exp_f32_e32 v19, v19
	v_lshlrev_b32_e32 v41, 16, v41
	v_lshlrev_b32_e32 v43, 16, v43
	v_add_f32_e32 v20, v33, v41
	v_add_f32_e32 v19, 1.0, v19
	v_rcp_f32_e32 v19, v19
	v_fma_f32 v20, v20, 0.5, -v37
	v_lshl_add_u32 v33, s0, 7, v51
	s_cselect_b32 s0, 4, 11
	v_fma_f32 v19, v19, -2.0, 1.0
	v_cndmask_b32_e64 v15, v15, v19, s[40:41]
	v_add_u32_e32 v15, 0x8000, v15
	ds_write_b16_d16_hi v18, v15 offset:4608
	v_add_f32_e32 v15, v35, v43
	v_fma_f32 v15, v15, 0.5, -v39
	v_fma_f32 v20, v11, v20, v37
	v_fma_f32 v15, v14, v15, v39
	s_mul_i32 s1, s0, 0x90
	v_lshlrev_b32_e32 v44, 16, v44
	v_add_u32_e32 v20, 0x8000, v20
	v_add_u32_e32 v15, 0x8000, v15
	v_add_u32_e32 v18, s1, v51
	ds_write_b16_d16_hi v33, v20 offset:13696
	ds_write_b16_d16_hi v18, v15 offset:2304
	v_add_f32_e32 v15, v36, v44
	v_fma_f32 v15, v15, 0.5, -v40
	v_fma_f32 v15, v13, v15, v40
	v_lshlrev_b32_e32 v58, 16, v58
	v_add_u32_e32 v15, 0x8000, v15
	ds_write_b16_d16_hi v18, v15
	v_add_f32_e32 v15, v38, v58
	v_fma_f32 v15, v15, 0.5, -v42
	v_fma_f32 v15, v12, v15, v42
	v_mul_f32_e32 v19, 0x4038aa3b, v15
	v_exp_f32_e32 v19, v19
	v_lshlrev_b32_e32 v45, 16, v45
	v_add_f32_e32 v20, v37, v45
	v_fma_f32 v20, v20, 0.5, -v41
	v_add_f32_e32 v19, 1.0, v19
	v_rcp_f32_e32 v19, v19
	v_fma_f32 v20, v11, v20, v41
	v_lshlrev_b32_e32 v63, 16, v63
	v_add_u32_e32 v20, 0x8000, v20
	v_fma_f32 v19, v19, -2.0, 1.0
	v_cndmask_b32_e64 v15, v15, v19, s[40:41]
	v_lshl_add_u32 v33, s0, 7, v51
	v_add_u32_e32 v15, 0x8000, v15
	ds_write_b16_d16_hi v33, v20 offset:13696
	ds_write_b16_d16_hi v18, v15 offset:4608
	v_add_f32_e32 v15, v39, v63
	s_cselect_b32 s0, 5, 10
	v_fma_f32 v15, v15, 0.5, -v43
	v_fma_f32 v15, v14, v15, v43
	s_mul_i32 s1, s0, 0x90
	v_lshlrev_b32_e32 v65, 16, v65
	v_add_u32_e32 v15, 0x8000, v15
	v_add_u32_e32 v18, s1, v51
	ds_write_b16_d16_hi v18, v15 offset:2304
	v_add_f32_e32 v15, v40, v65
	v_fma_f32 v15, v15, 0.5, -v44
	v_fma_f32 v15, v13, v15, v44
	v_lshlrev_b32_e32 v69, 16, v69
	v_add_u32_e32 v15, 0x8000, v15
	ds_write_b16_d16_hi v18, v15
	v_add_f32_e32 v15, v42, v69
	v_fma_f32 v15, v15, 0.5, -v58
	v_fma_f32 v15, v12, v15, v58
	v_mul_f32_e32 v19, 0x4038aa3b, v15
	v_exp_f32_e32 v19, v19
	v_lshlrev_b32_e32 v67, 16, v67
	v_lshlrev_b32_e32 v71, 16, v71
	v_add_f32_e32 v20, v41, v67
	v_add_f32_e32 v19, 1.0, v19
	v_rcp_f32_e32 v19, v19
	v_fma_f32 v20, v20, 0.5, -v45
	v_lshl_add_u32 v33, s0, 7, v51
	s_cselect_b32 s0, 6, 9
	v_fma_f32 v19, v19, -2.0, 1.0
	v_cndmask_b32_e64 v15, v15, v19, s[40:41]
	v_add_u32_e32 v15, 0x8000, v15
	ds_write_b16_d16_hi v18, v15 offset:4608
	v_add_f32_e32 v15, v43, v71
	v_fma_f32 v15, v15, 0.5, -v63
	v_fma_f32 v20, v11, v20, v45
	v_fma_f32 v15, v14, v15, v63
	s_mul_i32 s1, s0, 0x90
	v_lshlrev_b32_e32 v73, 16, v73
	v_add_u32_e32 v20, 0x8000, v20
	v_add_u32_e32 v15, 0x8000, v15
	v_add_u32_e32 v18, s1, v51
	ds_write_b16_d16_hi v33, v20 offset:13696
	ds_write_b16_d16_hi v18, v15 offset:2304
	v_add_f32_e32 v15, v44, v73
	v_fma_f32 v15, v15, 0.5, -v65
	v_fma_f32 v15, v13, v15, v65
	v_lshlrev_b32_e32 v75, 16, v75
	v_add_u32_e32 v15, 0x8000, v15
	ds_write_b16_d16_hi v18, v15
	v_add_f32_e32 v15, v58, v75
	v_fma_f32 v15, v15, 0.5, -v69
	v_fma_f32 v15, v12, v15, v69
	v_mul_f32_e32 v19, 0x4038aa3b, v15
	v_exp_f32_e32 v19, v19
	v_lshlrev_b32_e32 v74, 16, v74
	v_add_f32_e32 v20, v45, v74
	v_fma_f32 v20, v20, 0.5, -v67
	v_add_f32_e32 v19, 1.0, v19
	v_rcp_f32_e32 v19, v19
	v_fma_f32 v20, v11, v20, v67
	v_lshlrev_b32_e32 v76, 16, v76
	v_add_u32_e32 v20, 0x8000, v20
	v_fma_f32 v19, v19, -2.0, 1.0
	v_cndmask_b32_e64 v15, v15, v19, s[40:41]
	v_lshl_add_u32 v33, s0, 7, v51
	v_add_u32_e32 v15, 0x8000, v15
	ds_write_b16_d16_hi v33, v20 offset:13696
	ds_write_b16_d16_hi v18, v15 offset:4608
	v_add_f32_e32 v15, v63, v76
	s_cselect_b32 s0, 7, 8
	v_fma_f32 v15, v15, 0.5, -v71
	v_fma_f32 v15, v14, v15, v71
	s_mul_i32 s1, s0, 0x90
	v_lshlrev_b32_e32 v77, 16, v77
	v_add_u32_e32 v15, 0x8000, v15
	v_add_u32_e32 v18, s1, v51
	ds_write_b16_d16_hi v18, v15 offset:2304
	v_add_f32_e32 v15, v65, v77
	v_fma_f32 v15, v15, 0.5, -v73
	v_fma_f32 v15, v13, v15, v73
	v_lshlrev_b32_e32 v125, 16, v125
	v_add_u32_e32 v15, 0x8000, v15
	ds_write_b16_d16_hi v18, v15
	v_add_f32_e32 v15, v69, v125
	v_fma_f32 v15, v15, 0.5, -v75
	v_fma_f32 v15, v12, v15, v75
	v_mul_f32_e32 v19, 0x4038aa3b, v15
	v_exp_f32_e32 v19, v19
	v_lshlrev_b32_e32 v124, 16, v124
	v_lshlrev_b32_e32 v126, 16, v126
	v_add_f32_e32 v20, v67, v124
	v_add_f32_e32 v19, 1.0, v19
	v_rcp_f32_e32 v19, v19
	v_fma_f32 v20, v20, 0.5, -v74
	v_lshl_add_u32 v33, s0, 7, v51
	s_cselect_b32 s0, 8, 7
	v_fma_f32 v19, v19, -2.0, 1.0
	v_cndmask_b32_e64 v15, v15, v19, s[40:41]
	v_add_u32_e32 v15, 0x8000, v15
	ds_write_b16_d16_hi v18, v15 offset:4608
	v_add_f32_e32 v15, v71, v126
	v_fma_f32 v15, v15, 0.5, -v76
	v_fma_f32 v20, v11, v20, v74
	v_fma_f32 v15, v14, v15, v76
	s_mul_i32 s1, s0, 0x90
	v_lshlrev_b32_e32 v127, 16, v127
	v_add_u32_e32 v20, 0x8000, v20
	v_add_u32_e32 v15, 0x8000, v15
	v_add_u32_e32 v18, s1, v51
	ds_write_b16_d16_hi v33, v20 offset:13696
	ds_write_b16_d16_hi v18, v15 offset:2304
	v_add_f32_e32 v15, v73, v127
	v_fma_f32 v15, v15, 0.5, -v77
	v_fma_f32 v15, v13, v15, v77
	v_lshlrev_b32_e32 v129, 16, v129
	v_add_u32_e32 v15, 0x8000, v15
	ds_write_b16_d16_hi v18, v15
	v_add_f32_e32 v15, v75, v129
	v_fma_f32 v15, v15, 0.5, -v125
	v_fma_f32 v15, v12, v15, v125
	v_mul_f32_e32 v19, 0x4038aa3b, v15
	v_exp_f32_e32 v19, v19
	v_lshlrev_b32_e32 v128, 16, v128
	v_add_f32_e32 v20, v74, v128
	v_fma_f32 v20, v20, 0.5, -v124
	v_add_f32_e32 v19, 1.0, v19
	v_rcp_f32_e32 v19, v19
	v_fma_f32 v20, v11, v20, v124
	v_lshlrev_b32_e32 v130, 16, v130
	v_add_u32_e32 v20, 0x8000, v20
	v_fma_f32 v19, v19, -2.0, 1.0
	v_cndmask_b32_e64 v15, v15, v19, s[40:41]
	v_lshl_add_u32 v33, s0, 7, v51
	v_add_u32_e32 v15, 0x8000, v15
	ds_write_b16_d16_hi v33, v20 offset:13696
	ds_write_b16_d16_hi v18, v15 offset:4608
	v_add_f32_e32 v15, v76, v130
	s_cselect_b32 s0, 9, 6
	v_fma_f32 v15, v15, 0.5, -v126
	v_fma_f32 v15, v14, v15, v126
	s_mul_i32 s1, s0, 0x90
	v_lshlrev_b32_e32 v131, 16, v131
	v_add_u32_e32 v15, 0x8000, v15
	v_add_u32_e32 v18, s1, v51
	ds_write_b16_d16_hi v18, v15 offset:2304
	v_add_f32_e32 v15, v77, v131
	v_fma_f32 v15, v15, 0.5, -v127
	v_fma_f32 v15, v13, v15, v127
	v_lshlrev_b32_e32 v133, 16, v133
	v_add_u32_e32 v15, 0x8000, v15
	ds_write_b16_d16_hi v18, v15
	v_add_f32_e32 v15, v125, v133
	v_fma_f32 v15, v15, 0.5, -v129
	v_fma_f32 v15, v12, v15, v129
	v_mul_f32_e32 v19, 0x4038aa3b, v15
	v_exp_f32_e32 v19, v19
	v_lshlrev_b32_e32 v132, 16, v132
	v_lshlrev_b32_e32 v134, 16, v134
	v_add_f32_e32 v20, v124, v132
	v_add_f32_e32 v19, 1.0, v19
	v_rcp_f32_e32 v19, v19
	v_fma_f32 v20, v20, 0.5, -v128
	v_lshl_add_u32 v33, s0, 7, v51
	s_cselect_b32 s0, 10, 5
	v_fma_f32 v19, v19, -2.0, 1.0
	v_cndmask_b32_e64 v15, v15, v19, s[40:41]
	v_add_u32_e32 v15, 0x8000, v15
	ds_write_b16_d16_hi v18, v15 offset:4608
	v_add_f32_e32 v15, v126, v134
	v_fma_f32 v15, v15, 0.5, -v130
	v_fma_f32 v20, v11, v20, v128
	v_fma_f32 v15, v14, v15, v130
	s_mul_i32 s1, s0, 0x90
	v_lshlrev_b32_e32 v135, 16, v135
	v_add_u32_e32 v20, 0x8000, v20
	v_add_u32_e32 v15, 0x8000, v15
	v_add_u32_e32 v18, s1, v51
	ds_write_b16_d16_hi v33, v20 offset:13696
	ds_write_b16_d16_hi v18, v15 offset:2304
	v_add_f32_e32 v15, v127, v135
	v_fma_f32 v15, v15, 0.5, -v131
	v_fma_f32 v15, v13, v15, v131
	v_lshlrev_b32_e32 v137, 16, v137
	v_add_u32_e32 v15, 0x8000, v15
	ds_write_b16_d16_hi v18, v15
	v_add_f32_e32 v15, v129, v137
	v_fma_f32 v15, v15, 0.5, -v133
	v_fma_f32 v15, v12, v15, v133
	v_mul_f32_e32 v19, 0x4038aa3b, v15
	v_exp_f32_e32 v19, v19
	v_lshlrev_b32_e32 v136, 16, v136
	v_add_f32_e32 v20, v128, v136
	v_fma_f32 v20, v20, 0.5, -v132
	v_add_f32_e32 v19, 1.0, v19
	v_rcp_f32_e32 v19, v19
	v_fma_f32 v20, v11, v20, v132
	v_lshlrev_b32_e32 v138, 16, v138
	v_add_u32_e32 v20, 0x8000, v20
	v_fma_f32 v19, v19, -2.0, 1.0
	v_cndmask_b32_e64 v15, v15, v19, s[40:41]
	v_lshl_add_u32 v33, s0, 7, v51
	v_add_u32_e32 v15, 0x8000, v15
	ds_write_b16_d16_hi v33, v20 offset:13696
	ds_write_b16_d16_hi v18, v15 offset:4608
	v_add_f32_e32 v15, v130, v138
	s_cselect_b32 s0, 11, 4
	v_fma_f32 v15, v15, 0.5, -v134
	v_fma_f32 v15, v14, v15, v134
	s_mul_i32 s1, s0, 0x90
	v_lshlrev_b32_e32 v139, 16, v139
	v_add_u32_e32 v15, 0x8000, v15
	v_add_u32_e32 v18, s1, v51
	ds_write_b16_d16_hi v18, v15 offset:2304
	v_add_f32_e32 v15, v131, v139
	v_fma_f32 v15, v15, 0.5, -v135
	v_fma_f32 v15, v13, v15, v135
	s_waitcnt vmcnt(12)
	v_lshlrev_b32_e32 v32, 16, v141
	v_add_u32_e32 v15, 0x8000, v15
	ds_write_b16_d16_hi v18, v15
	v_add_f32_e32 v15, v133, v32
	v_fma_f32 v15, v15, 0.5, -v137
	v_fma_f32 v15, v12, v15, v137
	v_mul_f32_e32 v19, 0x4038aa3b, v15
	v_exp_f32_e32 v19, v19
	s_waitcnt vmcnt(11)
	v_lshlrev_b32_e32 v30, 16, v142
	v_add_f32_e32 v20, v132, v31
	v_fma_f32 v20, v20, 0.5, -v136
	v_add_f32_e32 v19, 1.0, v19
	v_rcp_f32_e32 v19, v19
	v_lshl_add_u32 v33, s0, 7, v51
	s_cselect_b32 s0, 12, 3
	v_fma_f32 v20, v11, v20, v136
	v_fma_f32 v19, v19, -2.0, 1.0
	v_cndmask_b32_e64 v15, v15, v19, s[40:41]
	v_add_u32_e32 v15, 0x8000, v15
	ds_write_b16_d16_hi v18, v15 offset:4608
	v_add_f32_e32 v15, v134, v30
	v_fma_f32 v15, v15, 0.5, -v138
	v_fma_f32 v15, v14, v15, v138
	s_mul_i32 s1, s0, 0x90
	s_waitcnt vmcnt(10)
	v_lshlrev_b32_e32 v29, 16, v143
	v_add_u32_e32 v20, 0x8000, v20
	v_add_u32_e32 v15, 0x8000, v15
	v_add_u32_e32 v18, s1, v51
	ds_write_b16_d16_hi v33, v20 offset:13696
	ds_write_b16_d16_hi v18, v15 offset:2304
	v_add_f32_e32 v15, v135, v29
	v_fma_f32 v15, v15, 0.5, -v139
	v_fma_f32 v15, v13, v15, v139
	s_waitcnt vmcnt(8)
	v_lshlrev_b32_e32 v28, 16, v145
	v_add_u32_e32 v15, 0x8000, v15
	ds_write_b16_d16_hi v18, v15
	v_add_f32_e32 v15, v137, v28
	v_fma_f32 v15, v15, 0.5, -v32
	v_fma_f32 v15, v12, v15, v32
	v_mul_f32_e32 v19, 0x4038aa3b, v15
	v_exp_f32_e32 v19, v19
	v_lshlrev_b32_e32 v27, 16, v144
	v_add_f32_e32 v20, v136, v27
	v_fma_f32 v20, v20, 0.5, -v31
	v_add_f32_e32 v19, 1.0, v19
	v_rcp_f32_e32 v19, v19
	v_fma_f32 v20, v11, v20, v31
	s_waitcnt vmcnt(7)
	v_lshlrev_b32_e32 v25, 16, v146
	v_add_u32_e32 v20, 0x8000, v20
	v_fma_f32 v19, v19, -2.0, 1.0
	v_cndmask_b32_e64 v15, v15, v19, s[40:41]
	v_lshl_add_u32 v33, s0, 7, v51
	v_add_u32_e32 v15, 0x8000, v15
	ds_write_b16_d16_hi v33, v20 offset:13696
	ds_write_b16_d16_hi v18, v15 offset:4608
	v_add_f32_e32 v15, v138, v25
	s_cselect_b32 s0, 13, 2
	v_fma_f32 v15, v15, 0.5, -v30
	v_fma_f32 v15, v14, v15, v30
	s_mul_i32 s1, s0, 0x90
	s_waitcnt vmcnt(6)
	v_lshlrev_b32_e32 v23, 16, v147
	v_add_u32_e32 v15, 0x8000, v15
	v_add_u32_e32 v18, s1, v51
	ds_write_b16_d16_hi v18, v15 offset:2304
	v_add_f32_e32 v15, v139, v23
	v_fma_f32 v15, v15, 0.5, -v29
	v_fma_f32 v15, v13, v15, v29
	s_waitcnt vmcnt(4)
	v_lshlrev_b32_e32 v22, 16, v149
	v_add_u32_e32 v15, 0x8000, v15
	ds_write_b16_d16_hi v18, v15
	v_add_f32_e32 v15, v32, v22
	v_fma_f32 v15, v15, 0.5, -v28
	v_fma_f32 v15, v12, v15, v28
	v_mul_f32_e32 v19, 0x4038aa3b, v15
	v_exp_f32_e32 v19, v19
	v_lshlrev_b32_e32 v21, 16, v148
	s_waitcnt vmcnt(3)
	v_lshlrev_b32_e32 v26, 16, v150
	v_add_f32_e32 v20, v31, v21
	v_add_f32_e32 v19, 1.0, v19
	v_rcp_f32_e32 v19, v19
	v_fma_f32 v20, v20, 0.5, -v27
	v_lshl_add_u32 v31, s0, 7, v51
	s_cselect_b32 s0, 14, 1
	v_fma_f32 v19, v19, -2.0, 1.0
	v_cndmask_b32_e64 v15, v15, v19, s[40:41]
	v_add_u32_e32 v15, 0x8000, v15
	ds_write_b16_d16_hi v18, v15 offset:4608
	v_add_f32_e32 v15, v30, v26
	v_fma_f32 v15, v15, 0.5, -v25
	v_fma_f32 v20, v11, v20, v27
	v_fma_f32 v15, v14, v15, v25
	s_mul_i32 s1, s0, 0x90
	s_waitcnt vmcnt(2)
	v_lshlrev_b32_e32 v24, 16, v151
	v_add_u32_e32 v20, 0x8000, v20
	v_add_u32_e32 v15, 0x8000, v15
	v_add_u32_e32 v18, s1, v51
	ds_write_b16_d16_hi v31, v20 offset:13696
	ds_write_b16_d16_hi v18, v15 offset:2304
	v_add_f32_e32 v15, v29, v24
	v_fma_f32 v15, v15, 0.5, -v23
	v_fma_f32 v15, v13, v15, v23
	s_waitcnt vmcnt(0)
	v_lshlrev_b32_e32 v17, 16, v17
	v_lshlrev_b32_e32 v5, 16, v5
	v_lshlrev_b32_e32 v16, 16, v16
	v_lshlrev_b32_e32 v4, 16, v4
	v_lshlrev_b32_e32 v2, 16, v153
	v_add_u32_e32 v15, 0x8000, v15
	ds_write_b16_d16_hi v18, v15
	v_add_f32_e32 v15, v28, v2
	v_fma_f32 v15, v15, 0.5, -v22
	v_fma_f32 v15, v12, v15, v22
	v_mul_f32_e32 v19, 0x4038aa3b, v15
	v_exp_f32_e32 v19, v19
	v_lshlrev_b32_e32 v3, 16, v152
	v_add_f32_e32 v20, v27, v3
	v_fma_f32 v20, v20, 0.5, -v21
	v_add_f32_e32 v19, 1.0, v19
	v_rcp_f32_e32 v19, v19
	v_fma_f32 v20, v11, v20, v21
	v_add_u32_e32 v20, 0x8000, v20
	v_lshl_add_u32 v27, s0, 7, v51
	v_fma_f32 v19, v19, -2.0, 1.0
	v_cndmask_b32_e64 v15, v15, v19, s[40:41]
	v_add_u32_e32 v15, 0x8000, v15
	v_add_f32_e32 v5, v5, v23
	ds_write_b16_d16_hi v27, v20 offset:13696
	ds_write_b16_d16_hi v18, v15 offset:4608
	s_cselect_b32 s0, 15, 0
	v_add_f32_e32 v15, v17, v25
	v_fma_f32 v5, v5, 0.5, -v24
	v_fma_f32 v15, v15, 0.5, -v26
	s_mul_i32 s1, s0, 0x90
	v_fmac_f32_e32 v24, v13, v5
	v_fmac_f32_e32 v26, v14, v15
	v_add_u32_e32 v15, s1, v51
	v_add_u32_e32 v5, 0x8000, v24
	ds_write_b16_d16_hi v15, v5
	v_add_f32_e32 v5, v16, v22
	v_fma_f32 v5, v5, 0.5, -v2
	v_fmac_f32_e32 v2, v12, v5
	v_mul_f32_e32 v5, 0x4038aa3b, v2
	v_exp_f32_e32 v5, v5
	v_add_f32_e32 v4, v4, v21
	v_fma_f32 v4, v4, 0.5, -v3
	v_fmac_f32_e32 v3, v11, v4
	v_add_f32_e32 v4, 1.0, v5
	v_rcp_f32_e32 v4, v4
	v_add_u32_e32 v3, 0x8000, v3
	v_lshl_add_u32 v5, s0, 7, v51
	ds_write_b16_d16_hi v5, v3 offset:13696
	v_fma_f32 v3, v4, -2.0, 1.0
	v_or_b32_e32 v11, s33, v47
	v_cndmask_b32_e64 v2, v2, v3, s[40:41]
	v_or_b32_e32 v40, s78, v11
	v_add_u32_e32 v14, 0x8000, v26
	v_add_u32_e32 v2, 0x8000, v2
	v_ashrrev_i32_e32 v41, 31, v40
	ds_write_b16_d16_hi v15, v14 offset:2304
	ds_write_b16_d16_hi v15, v2 offset:4608
	v_lshlrev_b64 v[20:21], 6, v[40:41]
	v_readlane_b32 s0, v253, 23
	s_waitcnt lgkmcnt(0)
	v_or_b32_e32 v20, v20, v118
	v_readlane_b32 s1, v253, 24
	v_readlane_b32 s2, v253, 27
	ds_read_b128 v[2:5], v55 offset:4608
	ds_read_b128 v[12:15], v55 offset:4672
	s_waitcnt lgkmcnt(0)
	v_lshl_add_u64 v[16:17], s[0:1], 0, v[20:21]
	v_readlane_b32 s3, v253, 28
	global_load_dwordx4 v[16:19], v[16:17], off
	v_or_b32_e32 v24, 16, v40
	v_lshl_add_u64 v[20:21], s[2:3], 0, v[20:21]
	global_load_dwordx4 v[20:23], v[20:21], off
	v_ashrrev_i32_e32 v25, 31, v24
	v_lshlrev_b64 v[28:29], 6, v[24:25]
	v_or_b32_e32 v28, v28, v118
	v_lshl_add_u64 v[24:25], s[0:1], 0, v[28:29]
	global_load_dwordx4 v[24:27], v[24:25], off
	v_lshl_add_u64 v[28:29], s[2:3], 0, v[28:29]
	global_load_dwordx4 v[28:31], v[28:29], off
	v_or_b32_e32 v32, 32, v40
	v_ashrrev_i32_e32 v33, 31, v32
	v_lshlrev_b64 v[36:37], 6, v[32:33]
	v_or_b32_e32 v36, v36, v118
	v_lshl_add_u64 v[32:33], s[0:1], 0, v[36:37]
	global_load_dwordx4 v[32:35], v[32:33], off
	v_lshl_add_u64 v[36:37], s[2:3], 0, v[36:37]
	global_load_dwordx4 v[36:39], v[36:37], off
	v_or_b32_e32 v40, 48, v40
	v_ashrrev_i32_e32 v41, 31, v40
	v_lshlrev_b64 v[44:45], 6, v[40:41]
	v_or_b32_e32 v44, v44, v118
	v_lshl_add_u64 v[40:41], s[0:1], 0, v[44:45]
	global_load_dwordx4 v[40:43], v[40:41], off
	v_lshl_add_u64 v[44:45], s[2:3], 0, v[44:45]
	global_load_dwordx4 v[74:77], v[44:45], off
	s_waitcnt vmcnt(7) lgkmcnt(1)
	v_mfma_f32_16x16x32_bf16 v[16:19], v[2:5], v[16:19], 0
	v_readlane_b32 s0, v253, 19
	v_readlane_b32 s1, v253, 20
	v_readlane_b32 s2, v253, 17
	s_waitcnt vmcnt(6) lgkmcnt(0)
	v_mfma_f32_16x16x32_bf16 v[20:23], v[12:15], v[20:23], 0
	s_nop 2
	v_add_u32_e32 v11, 0x8000, v16
	ds_write_b16_d16_hi v88, v11 offset:6912
	s_mov_b32 s4, 15
	s_mov_b32 s8, 0
	v_readlane_b32 s78, v251, 13
	v_add_u32_e32 v11, 0x8000, v20
	ds_write_b16_d16_hi v88, v11 offset:4608
	v_add_u32_e32 v11, 0x8000, v17
	ds_write_b16_d16_hi v89, v11 offset:6912
	v_add_u32_e32 v11, 0x8000, v21
	ds_write_b16_d16_hi v89, v11 offset:4608
	v_add_u32_e32 v11, 0x8000, v18
	ds_write_b16_d16_hi v90, v11 offset:6912
	v_add_u32_e32 v11, 0x8000, v22
	ds_write_b16_d16_hi v90, v11 offset:4608
	v_add_u32_e32 v11, 0x8000, v19
	s_waitcnt vmcnt(5)
	v_mfma_f32_16x16x32_bf16 v[16:19], v[2:5], v[24:27], 0
	ds_write_b16_d16_hi v92, v11 offset:6912
	v_add_u32_e32 v11, 0x8000, v23
	ds_write_b16_d16_hi v92, v11 offset:4608
	s_waitcnt vmcnt(4)
	v_mfma_f32_16x16x32_bf16 v[20:23], v[12:15], v[28:31], 0
	s_nop 2
	v_add_u32_e32 v11, 0x8000, v16
	ds_write_b16_d16_hi v93, v11 offset:6944
	s_nop 2
	v_add_u32_e32 v11, 0x8000, v20
	ds_write_b16_d16_hi v93, v11 offset:4640
	v_add_u32_e32 v11, 0x8000, v17
	ds_write_b16_d16_hi v89, v11 offset:6944
	v_add_u32_e32 v11, 0x8000, v21
	ds_write_b16_d16_hi v89, v11 offset:4640
	v_add_u32_e32 v11, 0x8000, v18
	ds_write_b16_d16_hi v91, v11 offset:6944
	v_add_u32_e32 v11, 0x8000, v22
	ds_write_b16_d16_hi v91, v11 offset:4640
	v_add_u32_e32 v11, 0x8000, v19
	s_waitcnt vmcnt(3)
	v_mfma_f32_16x16x32_bf16 v[16:19], v[2:5], v[32:35], 0
	ds_write_b16_d16_hi v92, v11 offset:6944
	v_add_u32_e32 v11, 0x8000, v23
	ds_write_b16_d16_hi v92, v11 offset:4640
	s_waitcnt vmcnt(2)
	v_mfma_f32_16x16x32_bf16 v[20:23], v[12:15], v[36:39], 0
	s_waitcnt vmcnt(1)
	v_mfma_f32_16x16x32_bf16 v[2:5], v[2:5], v[40:43], 0
	s_nop 0
	v_add_u32_e32 v11, 0x8000, v16
	ds_write_b16_d16_hi v93, v11 offset:6976
	s_nop 2
	v_add_u32_e32 v11, 0x8000, v20
	ds_write_b16_d16_hi v93, v11 offset:4672
	v_add_u32_e32 v11, 0x8000, v17
	ds_write_b16_d16_hi v89, v11 offset:6976
	v_add_u32_e32 v11, 0x8000, v21
	ds_write_b16_d16_hi v89, v11 offset:4672
	v_add_u32_e32 v11, 0x8000, v18
	s_waitcnt vmcnt(0)
	v_mfma_f32_16x16x32_bf16 v[12:15], v[12:15], v[74:77], 0
	ds_write_b16_d16_hi v91, v11 offset:6976
	v_add_u32_e32 v11, 0x8000, v22
	ds_write_b16_d16_hi v91, v11 offset:4672
	v_add_u32_e32 v11, 0x8000, v19
	ds_write_b16_d16_hi v92, v11 offset:6976
	v_add_u32_e32 v11, 0x8000, v23
	v_add_u32_e32 v2, 0x8000, v2
	ds_write_b16_d16_hi v92, v11 offset:4672
	ds_write_b16_d16_hi v93, v2 offset:7008
	v_add_u32_e32 v2, 0x8000, v12
	ds_write_b16_d16_hi v93, v2 offset:4704
	v_add_u32_e32 v2, 0x8000, v3
	ds_write_b16_d16_hi v89, v2 offset:7008
	v_add_u32_e32 v2, 0x8000, v13
	ds_write_b16_d16_hi v89, v2 offset:4704
	v_add_u32_e32 v2, 0x8000, v4
	ds_write_b16_d16_hi v91, v2 offset:7008
	v_add_u32_e32 v2, 0x8000, v14
	ds_write_b16_d16_hi v91, v2 offset:4704
	v_add_u32_e32 v2, 0x8000, v5
	ds_write_b16_d16_hi v92, v2 offset:7008
	v_add_u32_e32 v2, 0x8000, v15
	ds_write_b16_d16_hi v92, v2 offset:4704
	v_lshl_add_u64 v[2:3], s[0:1], 0, v[162:163]
	s_lshl_b32 s0, s20, 2
	s_ashr_i32 s1, s0, 31
	s_lshl_b64 s[0:1], s[0:1], 2
	s_add_u32 s0, s2, s0
	v_readlane_b32 s2, v253, 18
	s_waitcnt lgkmcnt(0)
	s_addc_u32 s1, s2, s1
	s_lshl_b32 s2, s11, 2
	s_add_u32 s9, s0, s2
	s_addc_u32 s11, s1, 0
	v_mov_b32_e32 v4, 1.0
	v_mov_b32_e32 v5, v51
	v_mov_b32_e32 v11, v117
	s_branch .LBB0_662
